# indexer passes: next tile's K-fragment request moved further up, right behind the four matrix ops that drain the current half's fragments
# baseline (speedup 1.0000x reference)
; __device__ __forceinline__ float relu_i(float p) { const int i = __float_as_int(p); return __int_as_float(i > 0 ? i : 0); }
; __device__ __forceinline__ void idx_scores_k(f32x16& sc, const bf16x8 (&kf)[4], const bf16x8 (&qf)[16], const f32x4& w) {
;     f32x16 p0 = f32x16{}, p1 = f32x16{};
; #pragma unroll
;     for (int d0 = 0; d0 < 4; ++d0) p0 = __builtin_amdgcn_mfma_f32_32x32x16_bf16(kf[d0], qf[d0], p0, 0, 0, 0);
; #pragma unroll
;     for (int d0 = 0; d0 < 4; ++d0) p1 = __builtin_amdgcn_mfma_f32_32x32x16_bf16(kf[d0], qf[4 + d0], p1, 0, 0, 0);
; #pragma unroll
;     for (int r = 0; r < 16; ++r) sc[r] = w[0] * relu_i(p0[r]);
;     p0 = f32x16{};
; #pragma unroll
;     for (int d0 = 0; d0 < 4; ++d0) p0 = __builtin_amdgcn_mfma_f32_32x32x16_bf16(kf[d0], qf[8 + d0], p0, 0, 0, 0);
; #pragma unroll
;     for (int r = 0; r < 16; ++r) sc[r] = fmaf(w[1], relu_i(p1[r]), sc[r]);
;     p1 = f32x16{};
; #pragma unroll
;     for (int d0 = 0; d0 < 4; ++d0) p1 = __builtin_amdgcn_mfma_f32_32x32x16_bf16(kf[d0], qf[12 + d0], p1, 0, 0, 0);
; #pragma unroll
;     for (int r = 0; r < 16; ++r) sc[r] = fmaf(w[2], relu_i(p0[r]), sc[r]);
; #pragma unroll
;     for (int r = 0; r < 16; ++r) sc[r] = fmaf(w[3], relu_i(p1[r]), sc[r]);
; }
; template <int PASS> __device__ __forceinline__ void idx_pass(const bf16_t* KIb, const bf16x8 (&qf)[16], const f32x4& w, int jd, int tq, int wid, int r32, int hi, unsigned khi, unsigned klo, bool cand, LAS unsigned char* L) {
;     ...
;     if (j <= jd) idx_loadk(kA, KIb + (size_t)(j * 64) * 64, r32, hi);
;     for (; j <= jd; j += 8) {
;         const bool diag = (j == jd);
;         idx_loadk(kB, KIb + (size_t)(j * 64 + 32) * 64, r32, hi);
;         f32x16 sc; idx_scores_k(sc, kA, qf, w);
;         unsigned lo, elo, hw, ehw;
;         if (diag) idx_half<PASS, true>(lo, elo, sc, j * 64, tq, r32, hi, khi, klo, cand, L); else idx_half<PASS, false>(lo, elo, sc, j * 64, tq, r32, hi, khi, klo, cand, L);
;         if (j + 8 <= jd) idx_loadk(kA, KIb + (size_t)((j + 8) * 64) * 64, r32, hi);
;         idx_scores_k(sc, kB, qf, w);
;         if (diag) idx_half<PASS, true>(hw, ehw, sc, j * 64 + 32, tq, r32, hi, khi, klo, cand, L); else idx_half<PASS, false>(hw, ehw, sc, j * 64 + 32, tq, r32, hi, khi, klo, cand, L);
.LBB0_750:
	s_and_b64 vcc, exec, s[14:15]
	s_waitcnt vmcnt(3)
	v_mfma_f32_32x32x16_bf16 v[2:17], v[46:49], v[70:73], 0
	s_waitcnt vmcnt(2)
	v_mfma_f32_32x32x16_bf16 v[2:17], v[42:45], v[74:77], v[2:17]
	s_waitcnt vmcnt(1)
	v_mfma_f32_32x32x16_bf16 v[2:17], v[38:41], v[78:81], v[2:17]
	s_waitcnt vmcnt(0)
	v_mfma_f32_32x32x16_bf16 v[2:17], v[34:37], v[82:85], v[2:17]
	s_cmp_gt_i32 s20, s65
	s_cbranch_scc1 .Lka_p1_skip
	s_ashr_i32 s11, s10, 31
	s_lshl_b64 s[0:1], s[10:11], 7
	v_lshl_add_u64 v[196:197], v[50:51], 0, s[0:1]
	global_load_dwordx4 v[18:21], v[196:197], off
	global_load_dwordx4 v[22:25], v[196:197], off offset:32
	global_load_dwordx4 v[26:29], v[196:197], off offset:64
	global_load_dwordx4 v[30:33], v[196:197], off offset:96
.Lka_p1_skip:
	v_mfma_f32_32x32x16_bf16 v[180:195], v[46:49], v[86:89], 0
	v_mfma_f32_32x32x16_bf16 v[180:195], v[42:45], v[90:93], v[180:195]
	v_mfma_f32_32x32x16_bf16 v[180:195], v[38:41], v[94:97], v[180:195]
	v_mfma_f32_32x32x16_bf16 v[180:195], v[34:37], v[98:101], v[180:195]
	s_nop 7
	v_max_i32_e32 v200, 0, v2
	v_fma_f32 v136, v66, v200, 0
	v_max_i32_e32 v200, 0, v3
	v_fma_f32 v135, v66, v200, 0
	v_max_i32_e32 v200, 0, v4
	v_fma_f32 v134, v66, v200, 0
	v_max_i32_e32 v200, 0, v5
	v_fma_f32 v65, v66, v200, 0
	v_max_i32_e32 v200, 0, v6
	v_fma_f32 v64, v66, v200, 0
	v_max_i32_e32 v200, 0, v7
	v_fma_f32 v63, v66, v200, 0
	v_max_i32_e32 v200, 0, v8
	v_fma_f32 v62, v66, v200, 0
	v_max_i32_e32 v200, 0, v9
	v_fma_f32 v61, v66, v200, 0
	v_max_i32_e32 v200, 0, v10
	v_fma_f32 v60, v66, v200, 0
	v_max_i32_e32 v200, 0, v11
	v_fma_f32 v59, v66, v200, 0
	v_max_i32_e32 v200, 0, v12
	v_fma_f32 v58, v66, v200, 0
	v_max_i32_e32 v200, 0, v13
	v_fma_f32 v57, v66, v200, 0
	v_max_i32_e32 v200, 0, v14
	v_fma_f32 v56, v66, v200, 0
	v_max_i32_e32 v200, 0, v15
	v_fma_f32 v55, v66, v200, 0
	v_max_i32_e32 v200, 0, v16
	v_fma_f32 v54, v66, v200, 0
	v_max_i32_e32 v200, 0, v17
	v_fma_f32 v53, v66, v200, 0
	v_mfma_f32_32x32x16_bf16 v[2:17], v[46:49], v[102:105], 0
	v_mfma_f32_32x32x16_bf16 v[2:17], v[42:45], v[106:109], v[2:17]
	v_mfma_f32_32x32x16_bf16 v[2:17], v[38:41], v[110:113], v[2:17]
	v_mfma_f32_32x32x16_bf16 v[2:17], v[34:37], v[114:117], v[2:17]
	v_max_i32_e32 v200, 0, v180
	v_fmac_f32_e32 v136, v67, v200
	v_max_i32_e32 v200, 0, v181
	v_fmac_f32_e32 v135, v67, v200
	v_max_i32_e32 v200, 0, v182
	v_fmac_f32_e32 v134, v67, v200
	v_max_i32_e32 v200, 0, v183
	v_fmac_f32_e32 v65, v67, v200
	v_max_i32_e32 v200, 0, v184
	v_fmac_f32_e32 v64, v67, v200
	v_max_i32_e32 v200, 0, v185
	v_fmac_f32_e32 v63, v67, v200
	v_max_i32_e32 v200, 0, v186
	v_fmac_f32_e32 v62, v67, v200
	v_max_i32_e32 v200, 0, v187
	v_fmac_f32_e32 v61, v67, v200
	v_max_i32_e32 v200, 0, v188
	v_fmac_f32_e32 v60, v67, v200
	v_max_i32_e32 v200, 0, v189
	v_fmac_f32_e32 v59, v67, v200
	v_max_i32_e32 v200, 0, v190
	v_fmac_f32_e32 v58, v67, v200
	v_max_i32_e32 v200, 0, v191
	v_fmac_f32_e32 v57, v67, v200
	v_max_i32_e32 v200, 0, v192
	v_fmac_f32_e32 v56, v67, v200
	v_max_i32_e32 v200, 0, v193
	v_fmac_f32_e32 v55, v67, v200
	v_max_i32_e32 v200, 0, v194
	v_fmac_f32_e32 v54, v67, v200
	v_max_i32_e32 v200, 0, v195
	v_fmac_f32_e32 v53, v67, v200
	v_mfma_f32_32x32x16_bf16 v[180:195], v[46:49], v[118:121], 0
	v_mfma_f32_32x32x16_bf16 v[180:195], v[42:45], v[122:125], v[180:195]
	v_mfma_f32_32x32x16_bf16 v[180:195], v[38:41], v[126:129], v[180:195]
	v_mfma_f32_32x32x16_bf16 v[180:195], v[34:37], v[130:133], v[180:195]
	v_max_i32_e32 v200, 0, v2
	v_fmac_f32_e32 v136, v68, v200
	v_max_i32_e32 v200, 0, v3
	v_fmac_f32_e32 v135, v68, v200
	v_max_i32_e32 v200, 0, v4
	v_fmac_f32_e32 v134, v68, v200
	v_max_i32_e32 v200, 0, v5
	v_fmac_f32_e32 v65, v68, v200
	v_max_i32_e32 v200, 0, v6
	v_fmac_f32_e32 v64, v68, v200
	v_max_i32_e32 v200, 0, v7
	v_fmac_f32_e32 v63, v68, v200
	v_max_i32_e32 v200, 0, v8
	v_fmac_f32_e32 v62, v68, v200
	v_max_i32_e32 v200, 0, v9
	v_fmac_f32_e32 v61, v68, v200
	v_max_i32_e32 v200, 0, v10
	v_fmac_f32_e32 v60, v68, v200
	v_max_i32_e32 v200, 0, v11
	v_fmac_f32_e32 v59, v68, v200
	v_max_i32_e32 v200, 0, v12
	v_fmac_f32_e32 v58, v68, v200
	v_max_i32_e32 v200, 0, v13
	v_fmac_f32_e32 v57, v68, v200
	v_max_i32_e32 v200, 0, v14
	v_fmac_f32_e32 v56, v68, v200
	v_max_i32_e32 v200, 0, v15
	v_fmac_f32_e32 v55, v68, v200
	v_max_i32_e32 v200, 0, v16
	v_fmac_f32_e32 v54, v68, v200
	v_max_i32_e32 v200, 0, v17
	v_fmac_f32_e32 v53, v68, v200
	v_max_i32_e32 v200, 0, v180
	v_fmac_f32_e32 v136, v69, v200
	v_max_i32_e32 v200, 0, v181
	v_fmac_f32_e32 v135, v69, v200
	v_max_i32_e32 v200, 0, v182
	v_fmac_f32_e32 v134, v69, v200
	v_max_i32_e32 v200, 0, v183
	v_fmac_f32_e32 v65, v69, v200
	v_max_i32_e32 v200, 0, v184
	v_fmac_f32_e32 v64, v69, v200
	v_max_i32_e32 v200, 0, v185
	v_fmac_f32_e32 v63, v69, v200
	v_max_i32_e32 v200, 0, v186
	v_fmac_f32_e32 v62, v69, v200
	v_max_i32_e32 v200, 0, v187
	v_fmac_f32_e32 v61, v69, v200
	v_max_i32_e32 v200, 0, v188
	v_fmac_f32_e32 v60, v69, v200
	v_max_i32_e32 v200, 0, v189
	v_fmac_f32_e32 v59, v69, v200
	v_max_i32_e32 v200, 0, v190
	v_fmac_f32_e32 v58, v69, v200
	v_max_i32_e32 v200, 0, v191
	v_fmac_f32_e32 v57, v69, v200
	v_max_i32_e32 v200, 0, v192
	v_fmac_f32_e32 v56, v69, v200
	v_max_i32_e32 v200, 0, v193
	v_fmac_f32_e32 v55, v69, v200
	v_max_i32_e32 v200, 0, v194
	v_fmac_f32_e32 v54, v69, v200
	v_max_i32_e32 v200, 0, v195
	v_fmac_f32_e32 v53, v69, v200
	s_cbranch_vccz .LBB0_752
; #define LAS __attribute__((address_space(3)))
; __device__ __forceinline__ int crow(int r, int hi) { return (r & 3) + 8 * (r >> 2) + 4 * hi; }
; __device__ __forceinline__ int ibin_u_m160(unsigned u) {
;     const int a = (int)u >> 20;
;     return imed3(-953 - a, 0, 159) + imed3(a - 936, 0, 158) + imed3((int)u, -160, 1);
; }
; template <int PASS, bool DIAG> __device__ __forceinline__ void idx_half(unsigned& bits, unsigned& ebits, const f32x16& sc, int sbase, int tq, int r32, int hi, unsigned khi, unsigned klo, bool cand, LAS unsigned char* L) {
;     ...
;     if (PASS == 1) {
;         LAS unsigned* H = (LAS unsigned*)(L + IL_HIST) + r32 * HSTR + 160;
; #pragma unroll
;         for (int r = 0; r < 16; ++r) { int b = ibin_u_m160(__float_as_uint(sc[r] + 0.0f)); asm("" : "+v"(b));
;             if (!DIAG || crow(r, 0) <= d) __hip_atomic_fetch_add(H + b, 1u, __ATOMIC_RELAXED, __HIP_MEMORY_SCOPE_WORKGROUP); }
	v_ashrrev_i32_e32 v3, 20, v136
	v_sub_u32_e32 v4, 0xfffffc47, v3
	v_med3_i32 v3, v3, s88, v233
	v_med3_i32 v2, v136, s89, 1
	v_med3_i32 v4, v4, 0, v232
	v_add3_u32 v2, v2, v3, v4
	v_lshl_add_u32 v2, v2, 2, v234
	ds_add_u32 v2, v229 offset:1152
	v_ashrrev_i32_e32 v3, 20, v135
	v_sub_u32_e32 v4, 0xfffffc47, v3
	v_med3_i32 v3, v3, s88, v233
	v_med3_i32 v2, v135, s89, 1
	v_med3_i32 v4, v4, 0, v232
	v_add_u32_e32 v2, v2, v3
	v_add3_u32 v2, v2, v4, s92
	s_mov_b64 s[14:15], -1
	v_lshl_add_u32 v2, v2, 2, v0
	ds_add_u32 v2, v229 offset:1152
	v_ashrrev_i32_e32 v3, 20, v134
	v_sub_u32_e32 v4, 0xfffffc47, v3
	v_med3_i32 v3, v3, s88, v233
	v_med3_i32 v2, v134, s89, 1
	v_med3_i32 v4, v4, 0, v232
	v_add3_u32 v2, v2, v3, v4
	v_lshl_add_u32 v2, v2, 2, v234
	ds_add_u32 v2, v229 offset:1152
	v_ashrrev_i32_e32 v3, 20, v65
	v_sub_u32_e32 v4, 0xfffffc47, v3
	v_med3_i32 v3, v3, s88, v233
	v_med3_i32 v2, v65, s89, 1
	v_med3_i32 v4, v4, 0, v232
	v_add3_u32 v2, v2, v3, v4
	v_lshl_add_u32 v2, v2, 2, v234
	ds_add_u32 v2, v229 offset:1152
	v_ashrrev_i32_e32 v3, 20, v64
	v_sub_u32_e32 v4, 0xfffffc47, v3
	v_med3_i32 v3, v3, s88, v233
	v_med3_i32 v2, v64, s89, 1
	v_med3_i32 v4, v4, 0, v232
	v_add3_u32 v2, v2, v3, v4
	v_lshl_add_u32 v2, v2, 2, v234
	ds_add_u32 v2, v229 offset:1152
	v_ashrrev_i32_e32 v3, 20, v63
	v_sub_u32_e32 v4, 0xfffffc47, v3
	v_med3_i32 v3, v3, s88, v233
	v_med3_i32 v2, v63, s89, 1
	v_med3_i32 v4, v4, 0, v232
	v_add3_u32 v2, v2, v3, v4
	v_lshl_add_u32 v2, v2, 2, v234
	ds_add_u32 v2, v229 offset:1152
	v_ashrrev_i32_e32 v3, 20, v62
	v_sub_u32_e32 v4, 0xfffffc47, v3
	v_med3_i32 v3, v3, s88, v233
	v_med3_i32 v2, v62, s89, 1
	v_med3_i32 v4, v4, 0, v232
	v_add3_u32 v2, v2, v3, v4
	v_lshl_add_u32 v2, v2, 2, v234
	ds_add_u32 v2, v229 offset:1152
	v_ashrrev_i32_e32 v3, 20, v61
	v_sub_u32_e32 v4, 0xfffffc47, v3
	v_med3_i32 v3, v3, s88, v233
	v_med3_i32 v2, v61, s89, 1
	v_med3_i32 v4, v4, 0, v232
	v_add3_u32 v2, v2, v3, v4
	v_lshl_add_u32 v2, v2, 2, v234
	ds_add_u32 v2, v229 offset:1152
	v_ashrrev_i32_e32 v3, 20, v60
	v_sub_u32_e32 v4, 0xfffffc47, v3
	v_med3_i32 v3, v3, s88, v233
	v_med3_i32 v2, v60, s89, 1
	v_med3_i32 v4, v4, 0, v232
	v_add3_u32 v2, v2, v3, v4
	v_lshl_add_u32 v2, v2, 2, v234
	ds_add_u32 v2, v229 offset:1152
	v_ashrrev_i32_e32 v3, 20, v59
	v_sub_u32_e32 v4, 0xfffffc47, v3
	v_med3_i32 v3, v3, s88, v233
	v_med3_i32 v2, v59, s89, 1
	v_med3_i32 v4, v4, 0, v232
	v_add3_u32 v2, v2, v3, v4
	v_lshl_add_u32 v2, v2, 2, v234
	ds_add_u32 v2, v229 offset:1152
	v_ashrrev_i32_e32 v3, 20, v58
	v_sub_u32_e32 v4, 0xfffffc47, v3
	v_med3_i32 v3, v3, s88, v233
	v_med3_i32 v2, v58, s89, 1
	v_med3_i32 v4, v4, 0, v232
	v_add3_u32 v2, v2, v3, v4
	v_lshl_add_u32 v2, v2, 2, v234
	ds_add_u32 v2, v229 offset:1152
	v_ashrrev_i32_e32 v3, 20, v57
	v_sub_u32_e32 v4, 0xfffffc47, v3
	v_med3_i32 v3, v3, s88, v233
	v_med3_i32 v2, v57, s89, 1
	v_med3_i32 v4, v4, 0, v232
	v_add3_u32 v2, v2, v3, v4
	v_lshl_add_u32 v2, v2, 2, v234
	ds_add_u32 v2, v229 offset:1152
	v_ashrrev_i32_e32 v3, 20, v56
	v_sub_u32_e32 v4, 0xfffffc47, v3
	v_med3_i32 v3, v3, s88, v233
	v_med3_i32 v2, v56, s89, 1
	v_med3_i32 v4, v4, 0, v232
	v_add3_u32 v2, v2, v3, v4
	v_lshl_add_u32 v2, v2, 2, v234
	ds_add_u32 v2, v229 offset:1152
	v_ashrrev_i32_e32 v3, 20, v55
	v_sub_u32_e32 v4, 0xfffffc47, v3
	v_med3_i32 v3, v3, s88, v233
	v_med3_i32 v2, v55, s89, 1
	v_med3_i32 v4, v4, 0, v232
	v_add3_u32 v2, v2, v3, v4
	v_lshl_add_u32 v2, v2, 2, v234
	ds_add_u32 v2, v229 offset:1152
	v_ashrrev_i32_e32 v3, 20, v54
	v_sub_u32_e32 v4, 0xfffffc47, v3
	v_med3_i32 v3, v3, s88, v233
	v_med3_i32 v2, v54, s89, 1
	v_med3_i32 v4, v4, 0, v232
	v_add3_u32 v2, v2, v3, v4
	v_lshl_add_u32 v2, v2, 2, v234
	ds_add_u32 v2, v229 offset:1152
	v_ashrrev_i32_e32 v3, 20, v53
	v_sub_u32_e32 v4, 0xfffffc47, v3
	v_med3_i32 v3, v3, s88, v233
	v_med3_i32 v2, v53, s89, 1
	v_med3_i32 v4, v4, 0, v232
	v_add_u32_e32 v2, v2, v3
	v_add3_u32 v3, v2, v4, s92
	s_cbranch_execz .LBB0_753
	s_branch .LBB0_784

; __device__ __forceinline__ float relu_i(float p) { const int i = __float_as_int(p); return __int_as_float(i > 0 ? i : 0); }
; __device__ __forceinline__ void idx_scores_k(f32x16& sc, const bf16x8 (&kf)[4], const bf16x8 (&qf)[16], const f32x4& w) {
;     f32x16 p0 = f32x16{}, p1 = f32x16{};
; #pragma unroll
;     for (int d0 = 0; d0 < 4; ++d0) p0 = __builtin_amdgcn_mfma_f32_32x32x16_bf16(kf[d0], qf[d0], p0, 0, 0, 0);
; #pragma unroll
;     for (int d0 = 0; d0 < 4; ++d0) p1 = __builtin_amdgcn_mfma_f32_32x32x16_bf16(kf[d0], qf[4 + d0], p1, 0, 0, 0);
; #pragma unroll
;     for (int r = 0; r < 16; ++r) sc[r] = w[0] * relu_i(p0[r]);
;     p0 = f32x16{};
; #pragma unroll
;     for (int d0 = 0; d0 < 4; ++d0) p0 = __builtin_amdgcn_mfma_f32_32x32x16_bf16(kf[d0], qf[8 + d0], p0, 0, 0, 0);
; #pragma unroll
;     for (int r = 0; r < 16; ++r) sc[r] = fmaf(w[1], relu_i(p1[r]), sc[r]);
;     p1 = f32x16{};
; #pragma unroll
;     for (int d0 = 0; d0 < 4; ++d0) p1 = __builtin_amdgcn_mfma_f32_32x32x16_bf16(kf[d0], qf[12 + d0], p1, 0, 0, 0);
; #pragma unroll
;     for (int r = 0; r < 16; ++r) sc[r] = fmaf(w[2], relu_i(p0[r]), sc[r]);
; #pragma unroll
;     for (int r = 0; r < 16; ++r) sc[r] = fmaf(w[3], relu_i(p1[r]), sc[r]);
; }
; template <int PASS> __device__ __forceinline__ void idx_pass(const bf16_t* KIb, const bf16x8 (&qf)[16], const f32x4& w, int jd, int tq, int wid, int r32, int hi, unsigned khi, unsigned klo, bool cand, LAS unsigned char* L) {
;     ...
;     if (j <= jd) idx_loadk(kA, KIb + (size_t)(j * 64) * 64, r32, hi);
;     for (; j <= jd; j += 8) {
;         const bool diag = (j == jd);
;         idx_loadk(kB, KIb + (size_t)(j * 64 + 32) * 64, r32, hi);
;         f32x16 sc; idx_scores_k(sc, kA, qf, w);
;         unsigned lo, elo, hw, ehw;
;         if (diag) idx_half<PASS, true>(lo, elo, sc, j * 64, tq, r32, hi, khi, klo, cand, L); else idx_half<PASS, false>(lo, elo, sc, j * 64, tq, r32, hi, khi, klo, cand, L);
;         if (j + 8 <= jd) idx_loadk(kA, KIb + (size_t)((j + 8) * 64) * 64, r32, hi);
;         idx_scores_k(sc, kB, qf, w);
;         if (diag) idx_half<PASS, true>(hw, ehw, sc, j * 64 + 32, tq, r32, hi, khi, klo, cand, L); else idx_half<PASS, false>(hw, ehw, sc, j * 64 + 32, tq, r32, hi, khi, klo, cand, L);
.LBB0_1130:
.LBB0_1131:
	s_mov_b64 s[14:15], -1
	s_and_b64 vcc, exec, s[18:19]
	s_waitcnt vmcnt(3)
	v_mfma_f32_32x32x16_bf16 v[2:17], v[46:49], v[70:73], 0
	s_waitcnt vmcnt(2)
	v_mfma_f32_32x32x16_bf16 v[2:17], v[42:45], v[74:77], v[2:17]
	s_waitcnt vmcnt(1)
	v_mfma_f32_32x32x16_bf16 v[2:17], v[38:41], v[78:81], v[2:17]
	s_waitcnt vmcnt(0)
	v_mfma_f32_32x32x16_bf16 v[2:17], v[34:37], v[82:85], v[2:17]
	s_cmp_gt_i32 s44, s65
	s_cbranch_scc1 .Lka_p2_skip
	s_ashr_i32 s17, s16, 31
	s_lshl_b64 s[0:1], s[16:17], 7
	v_lshl_add_u64 v[196:197], v[50:51], 0, s[0:1]
	global_load_dwordx4 v[18:21], v[196:197], off
	global_load_dwordx4 v[22:25], v[196:197], off offset:32
	global_load_dwordx4 v[26:29], v[196:197], off offset:64
	global_load_dwordx4 v[30:33], v[196:197], off offset:96
.Lka_p2_skip:
	v_mfma_f32_32x32x16_bf16 v[180:195], v[46:49], v[86:89], 0
	v_mfma_f32_32x32x16_bf16 v[180:195], v[42:45], v[90:93], v[180:195]
	v_mfma_f32_32x32x16_bf16 v[180:195], v[38:41], v[94:97], v[180:195]
	v_mfma_f32_32x32x16_bf16 v[180:195], v[34:37], v[98:101], v[180:195]
	s_nop 7
	v_max_i32_e32 v200, 0, v2
	v_fma_f32 v53, v66, v200, 0
	v_max_i32_e32 v200, 0, v3
	v_fma_f32 v54, v66, v200, 0
	v_max_i32_e32 v200, 0, v4
	v_fma_f32 v55, v66, v200, 0
	v_max_i32_e32 v200, 0, v5
	v_fma_f32 v56, v66, v200, 0
	v_max_i32_e32 v200, 0, v6
	v_fma_f32 v57, v66, v200, 0
	v_max_i32_e32 v200, 0, v7
	v_fma_f32 v58, v66, v200, 0
	v_max_i32_e32 v200, 0, v8
	v_fma_f32 v59, v66, v200, 0
	v_max_i32_e32 v200, 0, v9
	v_fma_f32 v60, v66, v200, 0
	v_max_i32_e32 v200, 0, v10
	v_fma_f32 v61, v66, v200, 0
	v_max_i32_e32 v200, 0, v11
	v_fma_f32 v62, v66, v200, 0
	v_max_i32_e32 v200, 0, v12
	v_fma_f32 v63, v66, v200, 0
	v_max_i32_e32 v200, 0, v13
	v_fma_f32 v64, v66, v200, 0
	v_max_i32_e32 v200, 0, v14
	v_fma_f32 v65, v66, v200, 0
	v_max_i32_e32 v200, 0, v15
	v_fma_f32 v144, v66, v200, 0
	v_max_i32_e32 v200, 0, v16
	v_fma_f32 v145, v66, v200, 0
	v_max_i32_e32 v200, 0, v17
	v_fma_f32 v146, v66, v200, 0
	v_mfma_f32_32x32x16_bf16 v[2:17], v[46:49], v[102:105], 0
	v_mfma_f32_32x32x16_bf16 v[2:17], v[42:45], v[106:109], v[2:17]
	v_mfma_f32_32x32x16_bf16 v[2:17], v[38:41], v[110:113], v[2:17]
	v_mfma_f32_32x32x16_bf16 v[2:17], v[34:37], v[114:117], v[2:17]
	v_max_i32_e32 v200, 0, v180
	v_fmac_f32_e32 v53, v67, v200
	v_max_i32_e32 v200, 0, v181
	v_fmac_f32_e32 v54, v67, v200
	v_max_i32_e32 v200, 0, v182
	v_fmac_f32_e32 v55, v67, v200
	v_max_i32_e32 v200, 0, v183
	v_fmac_f32_e32 v56, v67, v200
	v_max_i32_e32 v200, 0, v184
	v_fmac_f32_e32 v57, v67, v200
	v_max_i32_e32 v200, 0, v185
	v_fmac_f32_e32 v58, v67, v200
	v_max_i32_e32 v200, 0, v186
	v_fmac_f32_e32 v59, v67, v200
	v_max_i32_e32 v200, 0, v187
	v_fmac_f32_e32 v60, v67, v200
	v_max_i32_e32 v200, 0, v188
	v_fmac_f32_e32 v61, v67, v200
	v_max_i32_e32 v200, 0, v189
	v_fmac_f32_e32 v62, v67, v200
	v_max_i32_e32 v200, 0, v190
	v_fmac_f32_e32 v63, v67, v200
	v_max_i32_e32 v200, 0, v191
	v_fmac_f32_e32 v64, v67, v200
	v_max_i32_e32 v200, 0, v192
	v_fmac_f32_e32 v65, v67, v200
	v_max_i32_e32 v200, 0, v193
	v_fmac_f32_e32 v144, v67, v200
	v_max_i32_e32 v200, 0, v194
	v_fmac_f32_e32 v145, v67, v200
	v_max_i32_e32 v200, 0, v195
	v_fmac_f32_e32 v146, v67, v200
	v_mfma_f32_32x32x16_bf16 v[180:195], v[46:49], v[118:121], 0
	v_mfma_f32_32x32x16_bf16 v[180:195], v[42:45], v[122:125], v[180:195]
	v_mfma_f32_32x32x16_bf16 v[180:195], v[38:41], v[126:129], v[180:195]
	v_mfma_f32_32x32x16_bf16 v[180:195], v[34:37], v[130:133], v[180:195]
	v_max_i32_e32 v200, 0, v2
	v_fmac_f32_e32 v53, v68, v200
	v_max_i32_e32 v200, 0, v3
	v_fmac_f32_e32 v54, v68, v200
	v_max_i32_e32 v200, 0, v4
	v_fmac_f32_e32 v55, v68, v200
	v_max_i32_e32 v200, 0, v5
	v_fmac_f32_e32 v56, v68, v200
	v_max_i32_e32 v200, 0, v6
	v_fmac_f32_e32 v57, v68, v200
	v_max_i32_e32 v200, 0, v7
	v_fmac_f32_e32 v58, v68, v200
	v_max_i32_e32 v200, 0, v8
	v_fmac_f32_e32 v59, v68, v200
	v_max_i32_e32 v200, 0, v9
	v_fmac_f32_e32 v60, v68, v200
	v_max_i32_e32 v200, 0, v10
	v_fmac_f32_e32 v61, v68, v200
	v_max_i32_e32 v200, 0, v11
	v_fmac_f32_e32 v62, v68, v200
	v_max_i32_e32 v200, 0, v12
	v_fmac_f32_e32 v63, v68, v200
	v_max_i32_e32 v200, 0, v13
	v_fmac_f32_e32 v64, v68, v200
	v_max_i32_e32 v200, 0, v14
	v_fmac_f32_e32 v65, v68, v200
	v_max_i32_e32 v200, 0, v15
	v_fmac_f32_e32 v144, v68, v200
	v_max_i32_e32 v200, 0, v16
	v_fmac_f32_e32 v145, v68, v200
	v_max_i32_e32 v200, 0, v17
	v_fmac_f32_e32 v146, v68, v200
	v_max_i32_e32 v200, 0, v180
	v_fmac_f32_e32 v53, v69, v200
	v_max_i32_e32 v200, 0, v181
	v_fmac_f32_e32 v54, v69, v200
	v_max_i32_e32 v200, 0, v182
	v_fmac_f32_e32 v55, v69, v200
	v_max_i32_e32 v200, 0, v183
	v_fmac_f32_e32 v56, v69, v200
	v_max_i32_e32 v200, 0, v184
	v_fmac_f32_e32 v57, v69, v200
	v_max_i32_e32 v200, 0, v185
	v_fmac_f32_e32 v58, v69, v200
	v_max_i32_e32 v200, 0, v186
	v_fmac_f32_e32 v59, v69, v200
	v_max_i32_e32 v200, 0, v187
	v_fmac_f32_e32 v60, v69, v200
	v_max_i32_e32 v200, 0, v188
	v_fmac_f32_e32 v61, v69, v200
	v_max_i32_e32 v200, 0, v189
	v_fmac_f32_e32 v62, v69, v200
	v_max_i32_e32 v200, 0, v190
	v_fmac_f32_e32 v63, v69, v200
	v_max_i32_e32 v200, 0, v191
	v_fmac_f32_e32 v64, v69, v200
	v_max_i32_e32 v200, 0, v192
	v_fmac_f32_e32 v65, v69, v200
	v_max_i32_e32 v200, 0, v193
	v_fmac_f32_e32 v144, v69, v200
	v_max_i32_e32 v200, 0, v194
	v_fmac_f32_e32 v145, v69, v200
	v_max_i32_e32 v200, 0, v195
	v_fmac_f32_e32 v146, v69, v200
	s_cbranch_vccz .LBB0_1196
; #define LAS __attribute__((address_space(3)))
; __device__ __forceinline__ int crow(int r, int hi) { return (r & 3) + 8 * (r >> 2) + 4 * hi; }
; __device__ __forceinline__ unsigned fkey2(float v) { const unsigned u = __float_as_uint(v + 0.0f); return u ^ ((unsigned)((int)u >> 31) | 0x80000000u); }
; __device__ __forceinline__ void shl_ge(unsigned& acc, unsigned key, unsigned thr) { asm("v_cmp_ge_u32 vcc, %1, %2\n\tv_addc_co_u32 %0, vcc, %0, %0, vcc" : "+v"(acc) : "v"(key), "v"(thr) : "vcc"); }
; __device__ __forceinline__ unsigned spread4(unsigned x) { return (x & 0xFu) | ((x & 0xF0u) << 4) | ((x & 0xF00u) << 8) | ((x & 0xF000u) << 12); }
; template <int PASS, bool DIAG> __device__ __forceinline__ void idx_half(unsigned& bits, unsigned& ebits, const f32x16& sc, int sbase, int tq, int r32, int hi, unsigned khi, unsigned klo, bool cand, LAS unsigned char* L) {
;     ...
;         unsigned hb = 0u, lb = 0u;
; #pragma unroll
;         for (int r = 15; r >= 0; --r) { const unsigned key = fkey2(sc[r]); shl_ge(hb, key, khi); shl_ge(lb, key, klo); }
;         bits = spread4(hb); ebits = spread4(lb & ~hb);
;         if (DIAG) { const unsigned vm = d < 0 ? 0u : (d >= 31 ? 0xFFFFFFFFu : ((2u << d) - 1u)); bits &= vm; ebits &= vm; }
;         if (cand && ebits != 0u) {
;             unsigned slot = __hip_atomic_fetch_add((LAS unsigned*)(L + IL_CNT) + r32, (unsigned)__builtin_popcount(ebits), __ATOMIC_RELAXED, __HIP_MEMORY_SCOPE_WORKGROUP);
; #pragma unroll
;             for (int r = 0; r < 16; ++r) if ((ebits >> crow(r, 0)) & 1u) { const int s = sbase + crow(r, hi);
;                 if (slot < (unsigned)IDX_CAP) ((LAS unsigned long long*)(L + IL_CAND))[r32 * IDX_CAP + slot] = ((unsigned long long)fkey2(sc[r]) << 16) | (unsigned long long)(0xFFFFu - (unsigned)s);
;                 ++slot; }
	v_mov_b32_e32 v49, 0
	v_mov_b32_e32 v5, 0
	v_cmp_ge_f32 vcc, v146, v165
	v_addc_co_u32 v49, vcc, v49, v49, vcc
	v_cmp_ge_f32 vcc, v146, v164
	v_addc_co_u32 v5, vcc, v5, v5, vcc
	v_cmp_ge_f32 vcc, v145, v165
	v_addc_co_u32 v49, vcc, v49, v49, vcc
	v_cmp_ge_f32 vcc, v145, v164
	v_addc_co_u32 v5, vcc, v5, v5, vcc
	v_cmp_ge_f32 vcc, v144, v165
	v_addc_co_u32 v49, vcc, v49, v49, vcc
	v_cmp_ge_f32 vcc, v144, v164
	v_addc_co_u32 v5, vcc, v5, v5, vcc
	v_cmp_ge_f32 vcc, v65, v165
	v_addc_co_u32 v49, vcc, v49, v49, vcc
	v_cmp_ge_f32 vcc, v65, v164
	v_addc_co_u32 v5, vcc, v5, v5, vcc
	v_cmp_ge_f32 vcc, v64, v165
	v_addc_co_u32 v49, vcc, v49, v49, vcc
	v_cmp_ge_f32 vcc, v64, v164
	v_addc_co_u32 v5, vcc, v5, v5, vcc
	v_cmp_ge_f32 vcc, v63, v165
	v_addc_co_u32 v49, vcc, v49, v49, vcc
	v_cmp_ge_f32 vcc, v63, v164
	v_addc_co_u32 v5, vcc, v5, v5, vcc
	v_cmp_ge_f32 vcc, v62, v165
	v_addc_co_u32 v49, vcc, v49, v49, vcc
	v_cmp_ge_f32 vcc, v62, v164
	v_addc_co_u32 v5, vcc, v5, v5, vcc
	v_cmp_ge_f32 vcc, v61, v165
	v_addc_co_u32 v49, vcc, v49, v49, vcc
	v_cmp_ge_f32 vcc, v61, v164
	v_addc_co_u32 v5, vcc, v5, v5, vcc
	v_cmp_ge_f32 vcc, v60, v165
	v_addc_co_u32 v49, vcc, v49, v49, vcc
	v_cmp_ge_f32 vcc, v60, v164
	v_addc_co_u32 v5, vcc, v5, v5, vcc
	v_cmp_ge_f32 vcc, v59, v165
	v_addc_co_u32 v49, vcc, v49, v49, vcc
	v_cmp_ge_f32 vcc, v59, v164
	v_addc_co_u32 v5, vcc, v5, v5, vcc
	v_cmp_ge_f32 vcc, v58, v165
	v_addc_co_u32 v49, vcc, v49, v49, vcc
	v_cmp_ge_f32 vcc, v58, v164
	v_addc_co_u32 v5, vcc, v5, v5, vcc
	v_cmp_ge_f32 vcc, v57, v165
	v_addc_co_u32 v49, vcc, v49, v49, vcc
	v_cmp_ge_f32 vcc, v57, v164
	v_addc_co_u32 v5, vcc, v5, v5, vcc
	s_nop 0
	v_cmp_ge_f32 vcc, v56, v165
	v_addc_co_u32 v49, vcc, v49, v49, vcc
	s_nop 0
	v_cmp_ge_f32 vcc, v56, v164
	v_addc_co_u32 v5, vcc, v5, v5, vcc
	s_nop 0
	v_cmp_ge_f32 vcc, v55, v165
	v_addc_co_u32 v49, vcc, v49, v49, vcc
	s_nop 0
	v_cmp_ge_f32 vcc, v55, v164
	v_addc_co_u32 v5, vcc, v5, v5, vcc
	s_nop 0
	v_cmp_ge_f32 vcc, v54, v165
	v_addc_co_u32 v49, vcc, v49, v49, vcc
	s_nop 0
	v_cmp_ge_f32 vcc, v54, v164
	v_addc_co_u32 v5, vcc, v5, v5, vcc
	s_nop 0
	v_cmp_ge_f32 vcc, v53, v165
	v_addc_co_u32 v49, vcc, v49, v49, vcc
	s_nop 0
	v_cmp_ge_f32 vcc, v53, v164
	v_addc_co_u32 v5, vcc, v5, v5, vcc
	s_nop 0
	v_bitop3_b32 v3, v5, v49, v5 bitop3:0x30
	v_bitop3_b32 v5, v5, 15, v49 bitop3:0x40
	v_lshlrev_b32_e32 v7, 4, v3
	v_and_or_b32 v5, v7, s93, v5
	v_lshlrev_b32_e32 v7, 8, v3
	v_lshlrev_b32_e32 v9, 12, v3
	v_and_b32_e32 v7, 0xf0000, v7
	v_and_b32_e32 v9, 0xf000000, v9
	v_or3_b32 v48, v5, v7, v9
	v_cmp_ne_u32_e32 vcc, 0, v48
	s_and_b64 s[0:1], s[10:11], vcc
	s_and_saveexec_b64 s[18:19], s[0:1]
	s_cbranch_execz .LBB0_1195
	v_bcnt_u32_b32 v5, v48, 0
	ds_add_rtn_u32 v147, v221, v5
	v_and_b32_e32 v5, 1, v3
	v_cmp_eq_u32_e32 vcc, 1, v5
	s_and_saveexec_b64 s[14:15], vcc
	s_cbranch_execz .LBB0_1137
	s_waitcnt lgkmcnt(0)
	v_cmp_gt_u32_e32 vcc, s87, v147
	s_and_saveexec_b64 s[42:43], vcc
	s_cbranch_execz .LBB0_1136
	v_add_f32_e32 v0, 0, v53
	v_ashrrev_i32_e32 v252, 31, v0
	v_bitop3_b32 v0, v252, v0, s85 bitop3:0x36
	v_lshlrev_b64 v[148:149], 16, v[0:1]
	v_add_u32_e32 v0, s45, v142
	v_subrev_u32_e32 v0, 32, v0
	v_lshl_add_u32 v5, v147, 3, v136
	v_or_b32_e32 v148, v148, v0
	ds_write_b64 v5, v[148:149] offset:512
